# P0 MOD GEMV main loop: 2x unrolled, 8 row loads in flight instead of 4 (counted waits)
# baseline (speedup 1.0000x reference)
.LBB0_21:
	v_lshl_add_u64 v[42:43], v[34:35], 0, v[24:25]
	v_lshl_add_u64 v[46:47], v[32:33], 0, v[24:25]
	v_lshl_add_u64 v[50:51], v[30:31], 0, v[24:25]
	v_lshl_add_u64 v[54:55], v[28:29], 0, v[24:25]
	global_load_dwordx4 v[42:45], v[42:43], off nt
	s_nop 0
	global_load_dwordx4 v[46:49], v[46:47], off nt
	s_nop 0
	global_load_dwordx4 v[50:53], v[50:51], off nt
	s_nop 0
	global_load_dwordx4 v[54:57], v[54:55], off nt
	ds_read2_b32 v[58:59], v40 offset1:42
	v_add_u32_e32 v41, 0x2000, v40
	v_add_u32_e32 v70, 0x4000, v40
	v_add_u32_e32 v72, 0x6000, v40
	ds_read2_b32 v[60:61], v40 offset0:84 offset1:126
	ds_read2_b32 v[62:63], v41 offset1:42
	ds_read2_b32 v[64:65], v70 offset1:42
	ds_read2_b32 v[66:67], v72 offset1:42
	ds_read2_b32 v[68:69], v41 offset0:84 offset1:126
	ds_read2_b32 v[70:71], v70 offset0:84 offset1:126
	ds_read2_b32 v[72:73], v72 offset0:84 offset1:126
	s_waitcnt lgkmcnt(7)
	v_mov_b32_e32 v74, v59
	s_waitcnt lgkmcnt(5)
	v_mov_b32_e32 v78, v63
	s_waitcnt lgkmcnt(4)
	v_mov_b32_e32 v80, v65
	s_waitcnt lgkmcnt(3)
	v_mov_b32_e32 v82, v67
	v_add_u32_e32 v3, 0xa8, v3
	v_cmp_lt_i32_e64 s[8:9], s20, v3
	v_mov_b32_e32 v76, v61
	s_waitcnt lgkmcnt(2)
	v_mov_b32_e32 v84, v69
	s_waitcnt lgkmcnt(1)
	v_mov_b32_e32 v86, v71
	s_waitcnt lgkmcnt(0)
	v_mov_b32_e32 v88, v73
	v_lshl_add_u64 v[28:29], v[28:29], 0, s[44:45]
	v_lshl_add_u64 v[30:31], v[30:31], 0, s[44:45]
	v_lshl_add_u64 v[32:33], v[32:33], 0, s[44:45]
	v_add_u32_e32 v40, 0x2a0, v40
	v_lshl_add_u64 v[34:35], v[34:35], 0, s[44:45]
	s_or_b64 s[50:51], s[8:9], s[50:51]
	v_lshl_add_u64 v[90:91], v[34:35], 0, v[24:25]
	v_lshl_add_u64 v[94:95], v[32:33], 0, v[24:25]
	v_lshl_add_u64 v[98:99], v[30:31], 0, v[24:25]
	v_lshl_add_u64 v[102:103], v[28:29], 0, v[24:25]
	global_load_dwordx4 v[90:93], v[90:91], off nt
	s_nop 0
	global_load_dwordx4 v[94:97], v[94:95], off nt
	s_nop 0
	global_load_dwordx4 v[98:101], v[98:99], off nt
	s_nop 0
	global_load_dwordx4 v[102:105], v[102:103], off nt
	ds_read2_b32 v[106:107], v40 offset1:42
	v_add_u32_e32 v89, 0x2000, v40
	v_add_u32_e32 v118, 0x4000, v40
	v_add_u32_e32 v120, 0x6000, v40
	ds_read2_b32 v[108:109], v40 offset0:84 offset1:126
	ds_read2_b32 v[110:111], v89 offset1:42
	ds_read2_b32 v[112:113], v118 offset1:42
	ds_read2_b32 v[114:115], v120 offset1:42
	ds_read2_b32 v[116:117], v89 offset0:84 offset1:126
	ds_read2_b32 v[118:119], v118 offset0:84 offset1:126
	ds_read2_b32 v[120:121], v120 offset0:84 offset1:126
	s_waitcnt lgkmcnt(7)
	v_mov_b32_e32 v122, v107
	s_waitcnt lgkmcnt(5)
	v_mov_b32_e32 v126, v111
	s_waitcnt lgkmcnt(4)
	v_mov_b32_e32 v128, v113
	s_waitcnt lgkmcnt(3)
	v_mov_b32_e32 v130, v115
	v_add_u32_e32 v3, 0xa8, v3
	v_cmp_lt_i32_e64 s[8:9], s20, v3
	v_mov_b32_e32 v124, v109
	s_waitcnt lgkmcnt(2)
	v_mov_b32_e32 v132, v117
	s_waitcnt lgkmcnt(1)
	v_mov_b32_e32 v134, v119
	s_waitcnt lgkmcnt(0)
	v_mov_b32_e32 v136, v121
	v_lshl_add_u64 v[28:29], v[28:29], 0, s[44:45]
	v_lshl_add_u64 v[30:31], v[30:31], 0, s[44:45]
	v_lshl_add_u64 v[32:33], v[32:33], 0, s[44:45]
	v_add_u32_e32 v40, 0x2a0, v40
	v_lshl_add_u64 v[34:35], v[34:35], 0, s[44:45]
	s_or_b64 s[50:51], s[8:9], s[50:51]
	s_waitcnt vmcnt(7)
	v_pk_fma_f32 v[16:17], v[42:43], v[58:59], v[16:17] op_sel_hi:[1,0,1]
	v_pk_fma_f32 v[18:19], v[44:45], v[58:59], v[18:19] op_sel_hi:[1,0,1]
	v_pk_fma_f32 v[12:13], v[42:43], v[62:63], v[12:13] op_sel_hi:[1,0,1]
	v_pk_fma_f32 v[14:15], v[44:45], v[62:63], v[14:15] op_sel_hi:[1,0,1]
	v_pk_fma_f32 v[8:9], v[42:43], v[64:65], v[8:9] op_sel_hi:[1,0,1]
	v_pk_fma_f32 v[10:11], v[44:45], v[64:65], v[10:11] op_sel_hi:[1,0,1]
	v_pk_fma_f32 v[4:5], v[42:43], v[66:67], v[4:5] op_sel_hi:[1,0,1]
	v_pk_fma_f32 v[6:7], v[44:45], v[66:67], v[6:7] op_sel_hi:[1,0,1]
	s_waitcnt vmcnt(6)
	v_pk_fma_f32 v[18:19], v[48:49], v[74:75], v[18:19] op_sel_hi:[1,0,1]
	v_pk_fma_f32 v[16:17], v[46:47], v[74:75], v[16:17] op_sel_hi:[1,0,1]
	v_pk_fma_f32 v[14:15], v[48:49], v[78:79], v[14:15] op_sel_hi:[1,0,1]
	v_pk_fma_f32 v[12:13], v[46:47], v[78:79], v[12:13] op_sel_hi:[1,0,1]
	v_pk_fma_f32 v[10:11], v[48:49], v[80:81], v[10:11] op_sel_hi:[1,0,1]
	v_pk_fma_f32 v[8:9], v[46:47], v[80:81], v[8:9] op_sel_hi:[1,0,1]
	v_pk_fma_f32 v[6:7], v[48:49], v[82:83], v[6:7] op_sel_hi:[1,0,1]
	v_pk_fma_f32 v[4:5], v[46:47], v[82:83], v[4:5] op_sel_hi:[1,0,1]
	s_waitcnt vmcnt(5)
	v_pk_fma_f32 v[16:17], v[50:51], v[60:61], v[16:17] op_sel_hi:[1,0,1]
	v_pk_fma_f32 v[18:19], v[52:53], v[60:61], v[18:19] op_sel_hi:[1,0,1]
	v_pk_fma_f32 v[12:13], v[50:51], v[68:69], v[12:13] op_sel_hi:[1,0,1]
	v_pk_fma_f32 v[14:15], v[52:53], v[68:69], v[14:15] op_sel_hi:[1,0,1]
	v_pk_fma_f32 v[8:9], v[50:51], v[70:71], v[8:9] op_sel_hi:[1,0,1]
	v_pk_fma_f32 v[10:11], v[52:53], v[70:71], v[10:11] op_sel_hi:[1,0,1]
	v_pk_fma_f32 v[6:7], v[52:53], v[72:73], v[6:7] op_sel_hi:[1,0,1]
	v_pk_fma_f32 v[4:5], v[50:51], v[72:73], v[4:5] op_sel_hi:[1,0,1]
	s_waitcnt vmcnt(4)
	v_pk_fma_f32 v[18:19], v[56:57], v[76:77], v[18:19] op_sel_hi:[1,0,1]
	v_pk_fma_f32 v[16:17], v[54:55], v[76:77], v[16:17] op_sel_hi:[1,0,1]
	v_pk_fma_f32 v[14:15], v[56:57], v[84:85], v[14:15] op_sel_hi:[1,0,1]
	v_pk_fma_f32 v[12:13], v[54:55], v[84:85], v[12:13] op_sel_hi:[1,0,1]
	v_pk_fma_f32 v[10:11], v[56:57], v[86:87], v[10:11] op_sel_hi:[1,0,1]
	v_pk_fma_f32 v[8:9], v[54:55], v[86:87], v[8:9] op_sel_hi:[1,0,1]
	v_pk_fma_f32 v[6:7], v[56:57], v[88:89], v[6:7] op_sel_hi:[1,0,1]
	v_pk_fma_f32 v[4:5], v[54:55], v[88:89], v[4:5] op_sel_hi:[1,0,1]
	s_waitcnt vmcnt(3)
	v_pk_fma_f32 v[16:17], v[90:91], v[106:107], v[16:17] op_sel_hi:[1,0,1]
	v_pk_fma_f32 v[18:19], v[92:93], v[106:107], v[18:19] op_sel_hi:[1,0,1]
	v_pk_fma_f32 v[12:13], v[90:91], v[110:111], v[12:13] op_sel_hi:[1,0,1]
	v_pk_fma_f32 v[14:15], v[92:93], v[110:111], v[14:15] op_sel_hi:[1,0,1]
	v_pk_fma_f32 v[8:9], v[90:91], v[112:113], v[8:9] op_sel_hi:[1,0,1]
	v_pk_fma_f32 v[10:11], v[92:93], v[112:113], v[10:11] op_sel_hi:[1,0,1]
	v_pk_fma_f32 v[4:5], v[90:91], v[114:115], v[4:5] op_sel_hi:[1,0,1]
	v_pk_fma_f32 v[6:7], v[92:93], v[114:115], v[6:7] op_sel_hi:[1,0,1]
	s_waitcnt vmcnt(2)
	v_pk_fma_f32 v[18:19], v[96:97], v[122:123], v[18:19] op_sel_hi:[1,0,1]
	v_pk_fma_f32 v[16:17], v[94:95], v[122:123], v[16:17] op_sel_hi:[1,0,1]
	v_pk_fma_f32 v[14:15], v[96:97], v[126:127], v[14:15] op_sel_hi:[1,0,1]
	v_pk_fma_f32 v[12:13], v[94:95], v[126:127], v[12:13] op_sel_hi:[1,0,1]
	v_pk_fma_f32 v[10:11], v[96:97], v[128:129], v[10:11] op_sel_hi:[1,0,1]
	v_pk_fma_f32 v[8:9], v[94:95], v[128:129], v[8:9] op_sel_hi:[1,0,1]
	v_pk_fma_f32 v[6:7], v[96:97], v[130:131], v[6:7] op_sel_hi:[1,0,1]
	v_pk_fma_f32 v[4:5], v[94:95], v[130:131], v[4:5] op_sel_hi:[1,0,1]
	s_waitcnt vmcnt(1)
	v_pk_fma_f32 v[16:17], v[98:99], v[108:109], v[16:17] op_sel_hi:[1,0,1]
	v_pk_fma_f32 v[18:19], v[100:101], v[108:109], v[18:19] op_sel_hi:[1,0,1]
	v_pk_fma_f32 v[12:13], v[98:99], v[116:117], v[12:13] op_sel_hi:[1,0,1]
	v_pk_fma_f32 v[14:15], v[100:101], v[116:117], v[14:15] op_sel_hi:[1,0,1]
	v_pk_fma_f32 v[8:9], v[98:99], v[118:119], v[8:9] op_sel_hi:[1,0,1]
	v_pk_fma_f32 v[10:11], v[100:101], v[118:119], v[10:11] op_sel_hi:[1,0,1]
	v_pk_fma_f32 v[6:7], v[100:101], v[120:121], v[6:7] op_sel_hi:[1,0,1]
	v_pk_fma_f32 v[4:5], v[98:99], v[120:121], v[4:5] op_sel_hi:[1,0,1]
	s_waitcnt vmcnt(0)
	v_pk_fma_f32 v[18:19], v[104:105], v[124:125], v[18:19] op_sel_hi:[1,0,1]
	v_pk_fma_f32 v[16:17], v[102:103], v[124:125], v[16:17] op_sel_hi:[1,0,1]
	v_pk_fma_f32 v[14:15], v[104:105], v[132:133], v[14:15] op_sel_hi:[1,0,1]
	v_pk_fma_f32 v[12:13], v[102:103], v[132:133], v[12:13] op_sel_hi:[1,0,1]
	v_pk_fma_f32 v[10:11], v[104:105], v[134:135], v[10:11] op_sel_hi:[1,0,1]
	v_pk_fma_f32 v[8:9], v[102:103], v[134:135], v[8:9] op_sel_hi:[1,0,1]
	v_pk_fma_f32 v[6:7], v[104:105], v[136:137], v[6:7] op_sel_hi:[1,0,1]
	v_pk_fma_f32 v[4:5], v[102:103], v[136:137], v[4:5] op_sel_hi:[1,0,1]
	s_andn2_b64 exec, exec, s[50:51]
	s_cbranch_execnz .LBB0_21
	s_or_b64 exec, exec, s[50:51]
